# phase 4 q up-projection epilogue: rope table loads of 8 row groups preloaded together (two batches) instead of 16 dependent load-wait-rotate steps
# speedup vs baseline: 1.0038x; 1.0038x over previous
; DI unsigned pk_bf16(float lo, float hi) { f32x2 v = {lo, hi}; hbf16x2 r = __builtin_convertvector(v, hbf16x2); return __builtin_bit_cast(unsigned, r); }
;     DI void operator()(const f32x4 (&acc)[2][2][4][2], const pg8::GU& u, int wr, int wc, int fr, int fq) const {
;         const int row0 = u.pm * 256 + wr * 64 + fr;
; #pragma unroll
;         for (int bj = 0; bj < 2; ++bj) {
;             const int g32 = 8 * u.pn + 4 * bj + wc;
;             int axis, ibase; bool rot;
;             if (MODE == 0) { const int hg = g32 % 6; rot = hg >= 4; axis = hg - 4; ibase = 4 * fq; }
;             else { rot = u.pn < 5; axis = (g32 & 3) >> 1; ibase = 16 * (g32 & 1) + 4 * fq; }
;             const int col0 = 32 * g32 + 4 * fq;
; #pragma unroll
;             for (int ai = 0; ai < 2; ++ai)
; #pragma unroll
;                 for (int m = 0; m < 4; ++m) {
;                     const int row = row0 + ai * 128 + m * 16;
;                     f32x4 x1 = acc[ai][bj][m][0], x2 = acc[ai][bj][m][1];
;                     if (MODE == 0) { x1 *= 0.07216878364870322f * LOG2E; x2 *= 0.07216878364870322f * LOG2E; }
;                     if (rot && row >= NCTX) {
;                         const int t = (row - NCTX) & (SEQ - 1), pos = axis ? (t & 63) : (t >> 6);
;                         const f32x2* cs = R + pos * (MODE == 0 ? 16 : 32) + ibase;
;                         f32x4 o1, o2;
; #pragma unroll
;                         for (int j = 0; j < 4; ++j) { const f32x2 c = cs[j]; o1[j] = x1[j] * c[0] - x2[j] * c[1]; o2[j] = x2[j] * c[0] + x1[j] * c[1]; }
;                         x1 = o1; x2 = o2;
;                     }
;                     bf16_t* rowp = O + (size_t)row * ldc + col0;
;                     u32x2 w1, w2; w1.x = pk_bf16(x1[0], x1[1]); w1.y = pk_bf16(x1[2], x1[3]); w2.x = pk_bf16(x2[0], x2[1]); w2.y = pk_bf16(x2[2], x2[3]);
;                     *(u32x2*)(rowp) = w1; *(u32x2*)(rowp + 16) = w2;
;                 }
.LBB0_425:
	s_lshl_b32 s5, s12, 3
	s_or_b32 s67, s5, s84
	s_mul_hi_i32 s5, s67, 0x2aaaaaab
	s_lshr_b32 s6, s5, 31
	s_add_i32 s5, s5, s6
	s_lshl_b32 s4, s4, 8
	s_mul_i32 s5, s5, 6
	s_add_i32 s4, s4, s85
	s_sub_i32 s5, s67, s5
	s_cmp_gt_i32 s5, 3
	v_or_b32_e32 v165, s4, v1
	s_cselect_b64 s[72:73], -1, 0
	s_cmp_eq_u32 s5, 4
	s_cselect_b64 s[18:19], -1, 0
	s_bfe_u32 s4, s4, 0x50006
	v_cmp_lt_i32_e64 s[12:13], s90, v165
	s_xor_b32 s59, s4, 16
	v_pk_mul_f32 v[148:149], v[128:129], s[54:55] op_sel_hi:[1,0]
	v_pk_mul_f32 v[126:127], v[126:127], s[54:55] op_sel_hi:[1,0]
	v_pk_mul_f32 v[146:147], v[124:125], s[54:55] op_sel_hi:[1,0]
	v_pk_mul_f32 v[128:129], v[122:123], s[54:55] op_sel_hi:[1,0]
	s_and_b64 s[6:7], s[72:73], s[12:13]
	s_and_b64 s[4:5], exec, s[72:73]
	s_cbranch_scc0 .Lrope4_nopre_a
	v_add_u32_e32 v223, 0x80, v165
	v_lshrrev_b32_e32 v223, 6, v223
	v_bitop3_b32 v223, v223, 16, 31 bitop3:0x6c
	v_mov_b32_e32 v250, s59
	v_cndmask_b32_e64 v250, v1, v250, s[18:19]
	v_lshlrev_b32_e32 v134, 7, v250
	v_lshl_add_u64 v[248:249], v[136:137], 0, v[134:135]
	global_load_dwordx4 v[178:181], v[248:249], off
	global_load_dwordx4 v[182:185], v[248:249], off offset:16
	v_mov_b32_e32 v250, s59
	v_cndmask_b32_e64 v250, v158, v250, s[18:19]
	v_lshlrev_b32_e32 v134, 7, v250
	v_lshl_add_u64 v[248:249], v[136:137], 0, v[134:135]
	global_load_dwordx4 v[186:189], v[248:249], off
	global_load_dwordx4 v[190:193], v[248:249], off offset:16
	v_mov_b32_e32 v250, s59
	v_cndmask_b32_e64 v250, v159, v250, s[18:19]
	v_lshlrev_b32_e32 v134, 7, v250
	v_lshl_add_u64 v[248:249], v[136:137], 0, v[134:135]
	global_load_dwordx4 v[194:197], v[248:249], off
	global_load_dwordx4 v[198:201], v[248:249], off offset:16
	v_mov_b32_e32 v250, s59
	v_cndmask_b32_e64 v250, v160, v250, s[18:19]
	v_lshlrev_b32_e32 v134, 7, v250
	v_lshl_add_u64 v[248:249], v[136:137], 0, v[134:135]
	global_load_dwordx4 v[202:205], v[248:249], off
	global_load_dwordx4 v[206:209], v[248:249], off offset:16
	v_cndmask_b32_e64 v250, v1, v223, s[18:19]
	v_lshlrev_b32_e32 v134, 7, v250
	v_lshl_add_u64 v[248:249], v[136:137], 0, v[134:135]
	global_load_dwordx4 v[210:213], v[248:249], off
	global_load_dwordx4 v[214:217], v[248:249], off offset:16
	v_cndmask_b32_e64 v250, v158, v223, s[18:19]
	v_lshlrev_b32_e32 v134, 7, v250
	v_lshl_add_u64 v[248:249], v[136:137], 0, v[134:135]
	global_load_dwordx4 v[224:227], v[248:249], off
	global_load_dwordx4 v[228:231], v[248:249], off offset:16
	v_cndmask_b32_e64 v250, v159, v223, s[18:19]
	v_lshlrev_b32_e32 v134, 7, v250
	v_lshl_add_u64 v[248:249], v[136:137], 0, v[134:135]
	global_load_dwordx4 v[232:235], v[248:249], off
	global_load_dwordx4 v[236:239], v[248:249], off offset:16
	v_cndmask_b32_e64 v250, v160, v223, s[18:19]
	v_lshlrev_b32_e32 v134, 7, v250
	v_lshl_add_u64 v[248:249], v[136:137], 0, v[134:135]
	global_load_dwordx4 v[240:243], v[248:249], off
	global_load_dwordx4 v[244:247], v[248:249], off offset:16
.Lrope4_nopre_a:
	s_and_saveexec_b64 s[4:5], s[6:7]
	s_cbranch_execz .LBB0_427
	s_waitcnt vmcnt(14)
	v_mov_b32_e32 v170, v178
	v_mul_f32_e32 v122, v148, v182
	v_mul_f32_e32 v172, v146, v183
	v_mul_f32_e32 v166, v146, v182
	v_mul_f32_e32 v174, v148, v183
	v_mov_b32_e32 v146, v149
	v_mov_b32_e32 v148, v147
	v_mov_b32_e32 v171, v180
	v_mov_b32_e32 v124, v179
	v_pk_mul_f32 v[146:147], v[146:147], v[184:185]
	v_pk_mul_f32 v[148:149], v[148:149], v[184:185]
	v_mov_b32_e32 v125, v181
	v_pk_mul_f32 v[176:177], v[128:129], v[124:125]
	v_pk_mul_f32 v[124:125], v[126:127], v[124:125]
	v_mov_b32_e32 v123, v146
	v_mov_b32_e32 v173, v147
	v_mov_b32_e32 v167, v148
	v_mov_b32_e32 v175, v149
	v_pk_fma_f32 v[126:127], v[126:127], v[170:171], v[176:177] neg_lo:[0,0,1] neg_hi:[0,0,1]
	v_pk_fma_f32 v[128:129], v[128:129], v[170:171], v[124:125]
	v_pk_add_f32 v[148:149], v[122:123], v[172:173] neg_lo:[0,1] neg_hi:[0,1]
	v_pk_add_f32 v[146:147], v[166:167], v[174:175]
.LBB0_427:
	s_or_b64 exec, exec, s[4:5]
	v_lshl_or_b32 v124, s67, 5, v157
	v_mov_b64_e32 v[122:123], s[30:31]
	v_ashrrev_i32_e32 v125, 31, v124
	v_mad_i64_i32 v[122:123], s[4:5], v165, s91, v[122:123]
	v_lshl_add_u64 v[166:167], v[124:125], 1, v[122:123]
	v_cvt_pk_bf16_f32 v126, v126, v127
	v_cvt_pk_bf16_f32 v127, v148, v149
	v_cvt_pk_bf16_f32 v128, v128, v129
	v_cvt_pk_bf16_f32 v129, v146, v147
	global_store_dwordx2 v[166:167], v[126:127], off
	global_store_dwordx2 v[166:167], v[128:129], off offset:32
	v_or_b32_e32 v128, 16, v165
	v_cmp_lt_i32_e64 s[8:9], s90, v128
	v_pk_mul_f32 v[126:127], v[120:121], s[54:55] op_sel_hi:[1,0]
	v_pk_mul_f32 v[118:119], v[118:119], s[54:55] op_sel_hi:[1,0]
	v_pk_mul_f32 v[120:121], v[116:117], s[54:55] op_sel_hi:[1,0]
	v_pk_mul_f32 v[116:117], v[114:115], s[54:55] op_sel_hi:[1,0]
	s_and_b64 s[6:7], s[72:73], s[8:9]
	s_and_saveexec_b64 s[4:5], s[6:7]
	s_cbranch_execz .LBB0_429
	s_waitcnt vmcnt(14)
	v_mov_b32_e32 v114, v186
	v_mul_f32_e32 v146, v126, v190
	v_mul_f32_e32 v170, v120, v191
	v_mul_f32_e32 v166, v120, v190
	v_mul_f32_e32 v172, v126, v191
	v_mov_b32_e32 v120, v127
	v_mov_b32_e32 v126, v121
	v_mov_b32_e32 v115, v188
	v_mov_b32_e32 v148, v187
	v_pk_mul_f32 v[120:121], v[120:121], v[192:193]
	v_pk_mul_f32 v[126:127], v[126:127], v[192:193]
	v_mov_b32_e32 v149, v189
	v_pk_mul_f32 v[174:175], v[116:117], v[148:149]
	v_pk_mul_f32 v[148:149], v[118:119], v[148:149]
	v_mov_b32_e32 v147, v120
	v_mov_b32_e32 v171, v121
	v_mov_b32_e32 v167, v126
	v_mov_b32_e32 v173, v127
	v_pk_fma_f32 v[118:119], v[118:119], v[114:115], v[174:175] neg_lo:[0,0,1] neg_hi:[0,0,1]
	v_pk_fma_f32 v[116:117], v[116:117], v[114:115], v[148:149]
	v_pk_add_f32 v[126:127], v[146:147], v[170:171] neg_lo:[0,1] neg_hi:[0,1]
	v_pk_add_f32 v[120:121], v[166:167], v[172:173]
; DI unsigned pk_bf16(float lo, float hi) { f32x2 v = {lo, hi}; hbf16x2 r = __builtin_convertvector(v, hbf16x2); return __builtin_bit_cast(unsigned, r); }
;     DI void operator()(const f32x4 (&acc)[2][2][4][2], const pg8::GU& u, int wr, int wc, int fr, int fq) const {
;     ...
; #pragma unroll
;             for (int ai = 0; ai < 2; ++ai)
; #pragma unroll
;                 for (int m = 0; m < 4; ++m) {
;                     const int row = row0 + ai * 128 + m * 16;
;                     f32x4 x1 = acc[ai][bj][m][0], x2 = acc[ai][bj][m][1];
;                     if (MODE == 0) { x1 *= 0.07216878364870322f * LOG2E; x2 *= 0.07216878364870322f * LOG2E; }
;                     if (rot && row >= NCTX) {
;                         const int t = (row - NCTX) & (SEQ - 1), pos = axis ? (t & 63) : (t >> 6);
;                         const f32x2* cs = R + pos * (MODE == 0 ? 16 : 32) + ibase;
;                         f32x4 o1, o2;
; #pragma unroll
;                         for (int j = 0; j < 4; ++j) { const f32x2 c = cs[j]; o1[j] = x1[j] * c[0] - x2[j] * c[1]; o2[j] = x2[j] * c[0] + x1[j] * c[1]; }
;                         x1 = o1; x2 = o2;
;                     }
;                     bf16_t* rowp = O + (size_t)row * ldc + col0;
;                     u32x2 w1, w2; w1.x = pk_bf16(x1[0], x1[1]); w1.y = pk_bf16(x1[2], x1[3]); w2.x = pk_bf16(x2[0], x2[1]); w2.y = pk_bf16(x2[2], x2[3]);
;                     *(u32x2*)(rowp) = w1; *(u32x2*)(rowp + 16) = w2;
;                 }
.LBB0_429:
	s_or_b64 exec, exec, s[4:5]
	v_mov_b64_e32 v[114:115], s[30:31]
	v_mad_i64_i32 v[114:115], s[4:5], v128, s91, v[114:115]
	v_lshl_add_u64 v[128:129], v[124:125], 1, v[114:115]
	v_cvt_pk_bf16_f32 v118, v118, v119
	v_cvt_pk_bf16_f32 v119, v126, v127
	v_cvt_pk_bf16_f32 v116, v116, v117
	v_cvt_pk_bf16_f32 v117, v120, v121
	global_store_dwordx2 v[128:129], v[118:119], off
	global_store_dwordx2 v[128:129], v[116:117], off offset:32
	v_or_b32_e32 v118, 32, v165
	v_cmp_lt_i32_e64 s[4:5], s90, v118
	v_pk_mul_f32 v[116:117], v[112:113], s[54:55] op_sel_hi:[1,0]
	v_pk_mul_f32 v[110:111], v[110:111], s[54:55] op_sel_hi:[1,0]
	v_pk_mul_f32 v[112:113], v[108:109], s[54:55] op_sel_hi:[1,0]
	v_pk_mul_f32 v[108:109], v[106:107], s[54:55] op_sel_hi:[1,0]
	s_and_b64 s[10:11], s[72:73], s[4:5]
	s_and_saveexec_b64 s[6:7], s[10:11]
	s_cbranch_execz .LBB0_431
	s_waitcnt vmcnt(14)
	v_mov_b32_e32 v106, v194
	v_mul_f32_e32 v120, v116, v198
	v_mul_f32_e32 v126, v112, v199
	v_mul_f32_e32 v146, v112, v198
	v_mul_f32_e32 v166, v116, v199
	v_mov_b32_e32 v112, v117
	v_mov_b32_e32 v116, v113
	v_mov_b32_e32 v107, v196
	v_mov_b32_e32 v128, v195
	v_pk_mul_f32 v[112:113], v[112:113], v[200:201]
	v_pk_mul_f32 v[116:117], v[116:117], v[200:201]
	v_mov_b32_e32 v129, v197
	v_pk_mul_f32 v[168:169], v[108:109], v[128:129]
	v_pk_mul_f32 v[128:129], v[110:111], v[128:129]
	v_mov_b32_e32 v121, v112
	v_mov_b32_e32 v127, v113
	v_mov_b32_e32 v147, v116
	v_mov_b32_e32 v167, v117
	v_pk_fma_f32 v[110:111], v[110:111], v[106:107], v[168:169] neg_lo:[0,0,1] neg_hi:[0,0,1]
	v_pk_fma_f32 v[108:109], v[108:109], v[106:107], v[128:129]
	v_pk_add_f32 v[116:117], v[120:121], v[126:127] neg_lo:[0,1] neg_hi:[0,1]
	v_pk_add_f32 v[112:113], v[146:147], v[166:167]
.LBB0_431:
	s_or_b64 exec, exec, s[6:7]
	v_mov_b64_e32 v[106:107], s[30:31]
	v_mad_i64_i32 v[106:107], s[6:7], v118, s91, v[106:107]
	v_lshl_add_u64 v[118:119], v[124:125], 1, v[106:107]
	v_cvt_pk_bf16_f32 v110, v110, v111
	v_cvt_pk_bf16_f32 v111, v116, v117
	v_cvt_pk_bf16_f32 v108, v108, v109
	v_cvt_pk_bf16_f32 v109, v112, v113
	global_store_dwordx2 v[118:119], v[110:111], off
	global_store_dwordx2 v[118:119], v[108:109], off offset:32
	v_or_b32_e32 v110, 48, v165
	v_cmp_lt_i32_e32 vcc, s90, v110
	v_pk_mul_f32 v[104:105], v[104:105], s[54:55] op_sel_hi:[1,0]
	v_pk_mul_f32 v[102:103], v[102:103], s[54:55] op_sel_hi:[1,0]
	v_pk_mul_f32 v[108:109], v[100:101], s[54:55] op_sel_hi:[1,0]
	v_pk_mul_f32 v[100:101], v[98:99], s[54:55] op_sel_hi:[1,0]
	s_and_b64 s[10:11], s[72:73], vcc
	s_and_saveexec_b64 s[6:7], s[10:11]
	s_cbranch_execz .LBB0_433
	s_waitcnt vmcnt(14)
	v_mul_f32_e32 v146, v104, v207
	v_mov_b32_e32 v99, v204
	v_mov_b32_e32 v128, v203
	v_mov_b32_e32 v98, v202
	v_mov_b32_e32 v129, v205
	v_pk_mul_f32 v[112:113], v[100:101], v[128:129]
	v_pk_mul_f32 v[120:121], v[102:103], v[128:129]
	v_mul_f32_e32 v126, v104, v206
	v_mul_f32_e32 v128, v108, v207
	v_mul_f32_e32 v116, v108, v206
	v_mov_b32_e32 v108, v105
	v_pk_mul_f32 v[148:149], v[108:109], v[208:209]
	v_mov_b32_e32 v104, v109
	v_mov_b32_e32 v127, v148
	v_mov_b32_e32 v129, v149
	v_pk_mul_f32 v[104:105], v[104:105], v[208:209]
	v_pk_fma_f32 v[102:103], v[102:103], v[98:99], v[112:113] neg_lo:[0,0,1] neg_hi:[0,0,1]
	v_pk_add_f32 v[112:113], v[126:127], v[128:129] neg_lo:[0,1] neg_hi:[0,1]
	v_mov_b32_e32 v117, v104
	v_mov_b32_e32 v147, v105
	v_pk_fma_f32 v[100:101], v[100:101], v[98:99], v[120:121]
	v_pk_add_f32 v[108:109], v[116:117], v[146:147]
	v_mov_b32_e32 v104, v112
	v_mov_b32_e32 v105, v113
.LBB0_433:
	s_or_b64 exec, exec, s[6:7]
	v_mov_b64_e32 v[98:99], s[30:31]
	v_mad_i64_i32 v[98:99], s[6:7], v110, s91, v[98:99]
	v_lshl_add_u64 v[110:111], v[124:125], 1, v[98:99]
	v_cvt_pk_bf16_f32 v102, v102, v103
	v_cvt_pk_bf16_f32 v103, v104, v105
	v_cvt_pk_bf16_f32 v100, v100, v101
	v_cvt_pk_bf16_f32 v101, v108, v109
	global_store_dwordx2 v[110:111], v[102:103], off
	global_store_dwordx2 v[110:111], v[100:101], off offset:32
	v_add_u32_e32 v103, 0x80, v165
	s_movk_i32 s6, 0x37f
	v_lshrrev_b32_e32 v100, 6, v103
	v_cmp_lt_i32_e64 s[6:7], s6, v165
	v_bitop3_b32 v102, v100, 16, 31 bitop3:0x6c
	v_pk_mul_f32 v[96:97], v[96:97], s[54:55] op_sel_hi:[1,0]
	v_pk_mul_f32 v[94:95], v[94:95], s[54:55] op_sel_hi:[1,0]
	v_pk_mul_f32 v[100:101], v[92:93], s[54:55] op_sel_hi:[1,0]
	v_pk_mul_f32 v[92:93], v[90:91], s[54:55] op_sel_hi:[1,0]
	s_and_b64 s[14:15], s[72:73], s[6:7]
	s_and_saveexec_b64 s[10:11], s[14:15]
	s_cbranch_execz .LBB0_435
	s_waitcnt vmcnt(14)
	v_mul_f32_e32 v120, v96, v215
	v_mov_b32_e32 v91, v212
	v_mov_b32_e32 v118, v211
	v_mov_b32_e32 v90, v210
	v_mov_b32_e32 v119, v213
	v_pk_mul_f32 v[104:105], v[92:93], v[118:119]
	v_pk_mul_f32 v[112:113], v[94:95], v[118:119]
	v_mul_f32_e32 v116, v96, v214
	v_mul_f32_e32 v118, v100, v215
	v_mul_f32_e32 v108, v100, v214
	v_mov_b32_e32 v100, v97
	v_pk_mul_f32 v[126:127], v[100:101], v[216:217]
	v_mov_b32_e32 v96, v101
	v_mov_b32_e32 v117, v126
	v_mov_b32_e32 v119, v127
	v_pk_mul_f32 v[96:97], v[96:97], v[216:217]
	v_pk_fma_f32 v[94:95], v[94:95], v[90:91], v[104:105] neg_lo:[0,0,1] neg_hi:[0,0,1]
	v_pk_add_f32 v[104:105], v[116:117], v[118:119] neg_lo:[0,1] neg_hi:[0,1]
	v_mov_b32_e32 v109, v96
	v_mov_b32_e32 v121, v97
	v_pk_fma_f32 v[92:93], v[92:93], v[90:91], v[112:113]
	v_pk_add_f32 v[100:101], v[108:109], v[120:121]
	v_mov_b32_e32 v96, v104
	v_mov_b32_e32 v97, v105
; DI unsigned pk_bf16(float lo, float hi) { f32x2 v = {lo, hi}; hbf16x2 r = __builtin_convertvector(v, hbf16x2); return __builtin_bit_cast(unsigned, r); }
;     DI void operator()(const f32x4 (&acc)[2][2][4][2], const pg8::GU& u, int wr, int wc, int fr, int fq) const {
;     ...
; #pragma unroll
;             for (int ai = 0; ai < 2; ++ai)
; #pragma unroll
;                 for (int m = 0; m < 4; ++m) {
;                     const int row = row0 + ai * 128 + m * 16;
;                     f32x4 x1 = acc[ai][bj][m][0], x2 = acc[ai][bj][m][1];
;                     if (MODE == 0) { x1 *= 0.07216878364870322f * LOG2E; x2 *= 0.07216878364870322f * LOG2E; }
;                     if (rot && row >= NCTX) {
;                         const int t = (row - NCTX) & (SEQ - 1), pos = axis ? (t & 63) : (t >> 6);
;                         const f32x2* cs = R + pos * (MODE == 0 ? 16 : 32) + ibase;
;                         f32x4 o1, o2;
; #pragma unroll
;                         for (int j = 0; j < 4; ++j) { const f32x2 c = cs[j]; o1[j] = x1[j] * c[0] - x2[j] * c[1]; o2[j] = x2[j] * c[0] + x1[j] * c[1]; }
;                         x1 = o1; x2 = o2;
;                     }
;                     bf16_t* rowp = O + (size_t)row * ldc + col0;
;                     u32x2 w1, w2; w1.x = pk_bf16(x1[0], x1[1]); w1.y = pk_bf16(x1[2], x1[3]); w2.x = pk_bf16(x2[0], x2[1]); w2.y = pk_bf16(x2[2], x2[3]);
;                     *(u32x2*)(rowp) = w1; *(u32x2*)(rowp + 16) = w2;
;                 }
.LBB0_435:
	s_or_b64 exec, exec, s[10:11]
	v_mov_b64_e32 v[90:91], s[30:31]
	v_mad_i64_i32 v[90:91], s[10:11], v103, s91, v[90:91]
	s_movk_i32 s10, 0x36f
	v_lshl_add_u64 v[104:105], v[124:125], 1, v[90:91]
	v_cvt_pk_bf16_f32 v94, v94, v95
	v_cvt_pk_bf16_f32 v95, v96, v97
	v_cvt_pk_bf16_f32 v92, v92, v93
	v_cvt_pk_bf16_f32 v93, v100, v101
	v_cmp_lt_i32_e64 s[10:11], s10, v165
	global_store_dwordx2 v[104:105], v[94:95], off
	global_store_dwordx2 v[104:105], v[92:93], off offset:32
	v_pk_mul_f32 v[88:89], v[88:89], s[54:55] op_sel_hi:[1,0]
	v_pk_mul_f32 v[86:87], v[86:87], s[54:55] op_sel_hi:[1,0]
	v_pk_mul_f32 v[92:93], v[84:85], s[54:55] op_sel_hi:[1,0]
	v_pk_mul_f32 v[84:85], v[82:83], s[54:55] op_sel_hi:[1,0]
	s_and_b64 s[16:17], s[72:73], s[10:11]
	s_and_saveexec_b64 s[14:15], s[16:17]
	s_cbranch_execz .LBB0_437
	s_waitcnt vmcnt(14)
	v_mul_f32_e32 v112, v88, v229
	v_mov_b32_e32 v83, v226
	v_mov_b32_e32 v110, v225
	v_mov_b32_e32 v82, v224
	v_mov_b32_e32 v111, v227
	v_pk_mul_f32 v[100:101], v[84:85], v[110:111]
	v_pk_mul_f32 v[104:105], v[86:87], v[110:111]
	v_mul_f32_e32 v108, v88, v228
	v_mul_f32_e32 v110, v92, v229
	v_mul_f32_e32 v94, v92, v228
	v_mov_b32_e32 v92, v89
	v_pk_mul_f32 v[116:117], v[92:93], v[230:231]
	v_mov_b32_e32 v88, v93
	v_mov_b32_e32 v109, v116
	v_mov_b32_e32 v111, v117
	v_pk_mul_f32 v[88:89], v[88:89], v[230:231]
	v_pk_fma_f32 v[86:87], v[86:87], v[82:83], v[100:101] neg_lo:[0,0,1] neg_hi:[0,0,1]
	v_pk_add_f32 v[100:101], v[108:109], v[110:111] neg_lo:[0,1] neg_hi:[0,1]
	v_mov_b32_e32 v95, v88
	v_mov_b32_e32 v113, v89
	v_pk_fma_f32 v[84:85], v[84:85], v[82:83], v[104:105]
	v_pk_add_f32 v[92:93], v[94:95], v[112:113]
	v_mov_b32_e32 v88, v100
	v_mov_b32_e32 v89, v101
.LBB0_437:
	s_or_b64 exec, exec, s[14:15]
	v_add_u32_e32 v94, 0x90, v165
	v_mov_b64_e32 v[82:83], s[30:31]
	v_mad_i64_i32 v[82:83], s[14:15], v94, s91, v[82:83]
	s_movk_i32 s14, 0x35f
	v_lshl_add_u64 v[94:95], v[124:125], 1, v[82:83]
	v_cvt_pk_bf16_f32 v86, v86, v87
	v_cvt_pk_bf16_f32 v87, v88, v89
	v_cvt_pk_bf16_f32 v84, v84, v85
	v_cvt_pk_bf16_f32 v85, v92, v93
	v_cmp_lt_i32_e64 s[14:15], s14, v165
	global_store_dwordx2 v[94:95], v[86:87], off
	global_store_dwordx2 v[94:95], v[84:85], off offset:32
	v_pk_mul_f32 v[80:81], v[80:81], s[54:55] op_sel_hi:[1,0]
	v_pk_mul_f32 v[78:79], v[78:79], s[54:55] op_sel_hi:[1,0]
	v_pk_mul_f32 v[84:85], v[76:77], s[54:55] op_sel_hi:[1,0]
	v_pk_mul_f32 v[76:77], v[74:75], s[54:55] op_sel_hi:[1,0]
	s_and_b64 s[92:93], s[72:73], s[14:15]
	s_and_saveexec_b64 s[16:17], s[92:93]
	s_cbranch_execz .LBB0_439
	s_waitcnt vmcnt(14)
	v_mul_f32_e32 v96, v80, v236
	v_mul_f32_e32 v100, v84, v237
	v_mul_f32_e32 v86, v84, v236
	v_mov_b32_e32 v84, v81
	v_mov_b32_e32 v75, v234
	v_mov_b32_e32 v94, v233
	v_mul_f32_e32 v104, v80, v237
	v_pk_mul_f32 v[108:109], v[84:85], v[238:239]
	v_mov_b32_e32 v80, v85
	v_mov_b32_e32 v74, v232
	v_mov_b32_e32 v95, v235
	v_pk_mul_f32 v[92:93], v[76:77], v[94:95]
	v_mov_b32_e32 v97, v108
	v_mov_b32_e32 v101, v109
	v_pk_mul_f32 v[80:81], v[80:81], v[238:239]
	v_pk_mul_f32 v[94:95], v[78:79], v[94:95]
	v_pk_fma_f32 v[78:79], v[78:79], v[74:75], v[92:93] neg_lo:[0,0,1] neg_hi:[0,0,1]
	v_pk_add_f32 v[92:93], v[96:97], v[100:101] neg_lo:[0,1] neg_hi:[0,1]
	v_mov_b32_e32 v87, v80
	v_mov_b32_e32 v105, v81
	v_pk_fma_f32 v[76:77], v[76:77], v[74:75], v[94:95]
	v_pk_add_f32 v[84:85], v[86:87], v[104:105]
	v_mov_b32_e32 v80, v92
	v_mov_b32_e32 v81, v93
.LBB0_439:
	s_or_b64 exec, exec, s[16:17]
	v_add_u32_e32 v86, 0xa0, v165
	v_mov_b64_e32 v[74:75], s[30:31]
	v_mad_i64_i32 v[74:75], s[16:17], v86, s91, v[74:75]
	s_movk_i32 s16, 0x34f
	v_lshl_add_u64 v[86:87], v[124:125], 1, v[74:75]
	v_cvt_pk_bf16_f32 v78, v78, v79
	v_cvt_pk_bf16_f32 v79, v80, v81
	v_cvt_pk_bf16_f32 v76, v76, v77
	v_cvt_pk_bf16_f32 v77, v84, v85
	v_cmp_lt_i32_e64 s[16:17], s16, v165
	global_store_dwordx2 v[86:87], v[78:79], off
	global_store_dwordx2 v[86:87], v[76:77], off offset:32
	v_pk_mul_f32 v[72:73], v[72:73], s[54:55] op_sel_hi:[1,0]
	v_pk_mul_f32 v[70:71], v[70:71], s[54:55] op_sel_hi:[1,0]
	v_pk_mul_f32 v[76:77], v[68:69], s[54:55] op_sel_hi:[1,0]
	v_pk_mul_f32 v[68:69], v[66:67], s[54:55] op_sel_hi:[1,0]
	s_and_b64 s[92:93], s[72:73], s[16:17]
	s_and_saveexec_b64 s[72:73], s[92:93]
	s_cbranch_execz .LBB0_441
	s_waitcnt vmcnt(14)
	v_mul_f32_e32 v88, v72, v244
	v_mul_f32_e32 v92, v76, v245
	v_mul_f32_e32 v78, v76, v244
	v_mov_b32_e32 v76, v73
	v_mov_b32_e32 v67, v242
	v_mov_b32_e32 v86, v241
	v_mul_f32_e32 v94, v72, v245
	v_pk_mul_f32 v[96:97], v[76:77], v[246:247]
	v_mov_b32_e32 v72, v77
	v_mov_b32_e32 v66, v240
	v_mov_b32_e32 v87, v243
	v_pk_mul_f32 v[84:85], v[68:69], v[86:87]
	v_mov_b32_e32 v89, v96
	v_mov_b32_e32 v93, v97
	v_pk_mul_f32 v[72:73], v[72:73], v[246:247]
	v_pk_mul_f32 v[86:87], v[70:71], v[86:87]
	v_pk_fma_f32 v[70:71], v[70:71], v[66:67], v[84:85] neg_lo:[0,0,1] neg_hi:[0,0,1]
	v_pk_add_f32 v[84:85], v[88:89], v[92:93] neg_lo:[0,1] neg_hi:[0,1]
	v_mov_b32_e32 v79, v72
	v_mov_b32_e32 v95, v73
	v_pk_fma_f32 v[68:69], v[68:69], v[66:67], v[86:87]
	v_pk_add_f32 v[76:77], v[78:79], v[94:95]
	v_mov_b32_e32 v72, v84
	v_mov_b32_e32 v73, v85
; DI unsigned pk_bf16(float lo, float hi) { f32x2 v = {lo, hi}; hbf16x2 r = __builtin_convertvector(v, hbf16x2); return __builtin_bit_cast(unsigned, r); }
;     DI void operator()(const f32x4 (&acc)[2][2][4][2], const pg8::GU& u, int wr, int wc, int fr, int fq) const {
;     ...
;             int axis, ibase; bool rot;
;             if (MODE == 0) { const int hg = g32 % 6; rot = hg >= 4; axis = hg - 4; ibase = 4 * fq; }
;             else { rot = u.pn < 5; axis = (g32 & 3) >> 1; ibase = 16 * (g32 & 1) + 4 * fq; }
;             const int col0 = 32 * g32 + 4 * fq;
; #pragma unroll
;             for (int ai = 0; ai < 2; ++ai)
; #pragma unroll
;                 for (int m = 0; m < 4; ++m) {
;                     const int row = row0 + ai * 128 + m * 16;
;                     f32x4 x1 = acc[ai][bj][m][0], x2 = acc[ai][bj][m][1];
;                     if (MODE == 0) { x1 *= 0.07216878364870322f * LOG2E; x2 *= 0.07216878364870322f * LOG2E; }
;                     if (rot && row >= NCTX) {
;                         const int t = (row - NCTX) & (SEQ - 1), pos = axis ? (t & 63) : (t >> 6);
;                         const f32x2* cs = R + pos * (MODE == 0 ? 16 : 32) + ibase;
;                         f32x4 o1, o2;
; #pragma unroll
;                         for (int j = 0; j < 4; ++j) { const f32x2 c = cs[j]; o1[j] = x1[j] * c[0] - x2[j] * c[1]; o2[j] = x2[j] * c[0] + x1[j] * c[1]; }
;                         x1 = o1; x2 = o2;
;                     }
;                     bf16_t* rowp = O + (size_t)row * ldc + col0;
;                     u32x2 w1, w2; w1.x = pk_bf16(x1[0], x1[1]); w1.y = pk_bf16(x1[2], x1[3]); w2.x = pk_bf16(x2[0], x2[1]); w2.y = pk_bf16(x2[2], x2[3]);
;                     *(u32x2*)(rowp) = w1; *(u32x2*)(rowp + 16) = w2;
;                 }
.LBB0_441:
	s_or_b64 exec, exec, s[72:73]
	v_add_u32_e32 v78, 0xb0, v165
	v_mov_b64_e32 v[66:67], s[30:31]
	v_mad_i64_i32 v[66:67], s[18:19], v78, s91, v[66:67]
	s_or_b32 s67, s67, 4
	s_mul_hi_i32 s18, s67, 0x2aaaaaab
	s_lshr_b32 s19, s18, 31
	s_add_i32 s18, s18, s19
	s_mul_i32 s18, s18, 6
	s_sub_i32 s18, s67, s18
	s_cmp_gt_i32 s18, 3
	v_lshl_add_u64 v[78:79], v[124:125], 1, v[66:67]
	v_cvt_pk_bf16_f32 v70, v70, v71
	v_cvt_pk_bf16_f32 v71, v72, v73
	v_cvt_pk_bf16_f32 v68, v68, v69
	v_cvt_pk_bf16_f32 v69, v76, v77
	s_cselect_b64 s[72:73], -1, 0
	s_cmp_eq_u32 s18, 4
	global_store_dwordx2 v[78:79], v[70:71], off
	global_store_dwordx2 v[78:79], v[68:69], off offset:32
	s_cselect_b64 s[18:19], -1, 0
	v_pk_mul_f32 v[64:65], v[64:65], s[54:55] op_sel_hi:[1,0]
	v_pk_mul_f32 v[62:63], v[62:63], s[54:55] op_sel_hi:[1,0]
	v_pk_mul_f32 v[68:69], v[60:61], s[54:55] op_sel_hi:[1,0]
	v_pk_mul_f32 v[60:61], v[58:59], s[54:55] op_sel_hi:[1,0]
	s_and_b64 s[92:93], s[72:73], s[12:13]
	s_and_b64 s[12:13], exec, s[72:73]
	s_cbranch_scc0 .Lrope4_nopre_b
	v_add_u32_e32 v223, 0x80, v165
	v_lshrrev_b32_e32 v223, 6, v223
	v_bitop3_b32 v223, v223, 16, 31 bitop3:0x6c
	v_mov_b32_e32 v250, s59
	v_cndmask_b32_e64 v250, v1, v250, s[18:19]
	v_lshlrev_b32_e32 v134, 7, v250
	v_lshl_add_u64 v[248:249], v[136:137], 0, v[134:135]
	global_load_dwordx4 v[178:181], v[248:249], off
	global_load_dwordx4 v[182:185], v[248:249], off offset:16
	v_mov_b32_e32 v250, s59
	v_cndmask_b32_e64 v250, v158, v250, s[18:19]
	v_lshlrev_b32_e32 v134, 7, v250
	v_lshl_add_u64 v[248:249], v[136:137], 0, v[134:135]
	global_load_dwordx4 v[186:189], v[248:249], off
	global_load_dwordx4 v[190:193], v[248:249], off offset:16
	v_mov_b32_e32 v250, s59
	v_cndmask_b32_e64 v250, v159, v250, s[18:19]
	v_lshlrev_b32_e32 v134, 7, v250
	v_lshl_add_u64 v[248:249], v[136:137], 0, v[134:135]
	global_load_dwordx4 v[194:197], v[248:249], off
	global_load_dwordx4 v[198:201], v[248:249], off offset:16
	v_mov_b32_e32 v250, s59
	v_cndmask_b32_e64 v250, v160, v250, s[18:19]
	v_lshlrev_b32_e32 v134, 7, v250
	v_lshl_add_u64 v[248:249], v[136:137], 0, v[134:135]
	global_load_dwordx4 v[202:205], v[248:249], off
	global_load_dwordx4 v[206:209], v[248:249], off offset:16
	v_cndmask_b32_e64 v250, v1, v223, s[18:19]
	v_lshlrev_b32_e32 v134, 7, v250
	v_lshl_add_u64 v[248:249], v[136:137], 0, v[134:135]
	global_load_dwordx4 v[210:213], v[248:249], off
	global_load_dwordx4 v[214:217], v[248:249], off offset:16
	v_cndmask_b32_e64 v250, v158, v223, s[18:19]
	v_lshlrev_b32_e32 v134, 7, v250
	v_lshl_add_u64 v[248:249], v[136:137], 0, v[134:135]
	global_load_dwordx4 v[224:227], v[248:249], off
	global_load_dwordx4 v[228:231], v[248:249], off offset:16
	v_cndmask_b32_e64 v250, v159, v223, s[18:19]
	v_lshlrev_b32_e32 v134, 7, v250
	v_lshl_add_u64 v[248:249], v[136:137], 0, v[134:135]
	global_load_dwordx4 v[232:235], v[248:249], off
	global_load_dwordx4 v[236:239], v[248:249], off offset:16
	v_cndmask_b32_e64 v250, v160, v223, s[18:19]
	v_lshlrev_b32_e32 v134, 7, v250
	v_lshl_add_u64 v[248:249], v[136:137], 0, v[134:135]
	global_load_dwordx4 v[240:243], v[248:249], off
	global_load_dwordx4 v[244:247], v[248:249], off offset:16
.Lrope4_nopre_b:
	s_and_saveexec_b64 s[12:13], s[92:93]
	s_cbranch_execz .LBB0_443
	s_waitcnt vmcnt(14)
	v_mul_f32_e32 v80, v64, v182
	v_mul_f32_e32 v84, v68, v183
	v_mul_f32_e32 v70, v68, v182
	v_mov_b32_e32 v68, v65
	v_mov_b32_e32 v59, v180
	v_mov_b32_e32 v78, v179
	v_mul_f32_e32 v86, v64, v183
	v_pk_mul_f32 v[88:89], v[68:69], v[184:185]
	v_mov_b32_e32 v64, v69
	v_mov_b32_e32 v58, v178
	v_mov_b32_e32 v79, v181
	v_pk_mul_f32 v[76:77], v[60:61], v[78:79]
	v_mov_b32_e32 v81, v88
	v_mov_b32_e32 v85, v89
	v_pk_mul_f32 v[64:65], v[64:65], v[184:185]
	v_pk_mul_f32 v[78:79], v[62:63], v[78:79]
	v_pk_fma_f32 v[62:63], v[62:63], v[58:59], v[76:77] neg_lo:[0,0,1] neg_hi:[0,0,1]
	v_pk_add_f32 v[76:77], v[80:81], v[84:85] neg_lo:[0,1] neg_hi:[0,1]
	v_mov_b32_e32 v71, v64
	v_mov_b32_e32 v87, v65
	v_pk_fma_f32 v[60:61], v[60:61], v[58:59], v[78:79]
	v_pk_add_f32 v[68:69], v[70:71], v[86:87]
	v_mov_b32_e32 v64, v76
	v_mov_b32_e32 v65, v77
.LBB0_443:
	s_or_b64 exec, exec, s[12:13]
	v_lshl_or_b32 v58, s67, 5, v157
	v_ashrrev_i32_e32 v59, 31, v58
	v_lshl_add_u64 v[70:71], v[58:59], 1, v[122:123]
	v_cvt_pk_bf16_f32 v62, v62, v63
	v_cvt_pk_bf16_f32 v63, v64, v65
	v_pk_mul_f32 v[56:57], v[56:57], s[54:55] op_sel_hi:[1,0]
	v_pk_mul_f32 v[54:55], v[54:55], s[54:55] op_sel_hi:[1,0]
	v_pk_mul_f32 v[52:53], v[52:53], s[54:55] op_sel_hi:[1,0]
	v_pk_mul_f32 v[50:51], v[50:51], s[54:55] op_sel_hi:[1,0]
	s_and_b64 s[12:13], s[72:73], s[8:9]
	v_cvt_pk_bf16_f32 v60, v60, v61
	v_cvt_pk_bf16_f32 v61, v68, v69
	global_store_dwordx2 v[70:71], v[62:63], off
	global_store_dwordx2 v[70:71], v[60:61], off offset:32
	s_and_saveexec_b64 s[8:9], s[12:13]
	s_cbranch_execz .LBB0_445
	s_waitcnt vmcnt(14)
	v_mul_f32_e32 v72, v56, v190
	v_mul_f32_e32 v76, v52, v191
	v_mul_f32_e32 v60, v52, v190
	v_mov_b32_e32 v52, v57
	v_mov_b32_e32 v65, v188
	v_mov_b32_e32 v70, v187
	v_mul_f32_e32 v78, v56, v191
	v_pk_mul_f32 v[80:81], v[52:53], v[192:193]
	v_mov_b32_e32 v56, v53
	v_mov_b32_e32 v64, v186
	v_mov_b32_e32 v71, v189
	v_pk_mul_f32 v[68:69], v[50:51], v[70:71]
	v_mov_b32_e32 v73, v80
	v_mov_b32_e32 v77, v81
	v_pk_mul_f32 v[52:53], v[56:57], v[192:193]
	v_pk_mul_f32 v[70:71], v[54:55], v[70:71]
	v_pk_fma_f32 v[54:55], v[54:55], v[64:65], v[68:69] neg_lo:[0,0,1] neg_hi:[0,0,1]
	v_pk_add_f32 v[68:69], v[72:73], v[76:77] neg_lo:[0,1] neg_hi:[0,1]
	v_mov_b32_e32 v61, v52
	v_mov_b32_e32 v79, v53
	v_pk_fma_f32 v[50:51], v[50:51], v[64:65], v[70:71]
	v_pk_add_f32 v[52:53], v[60:61], v[78:79]
	v_mov_b32_e32 v56, v68
	v_mov_b32_e32 v57, v69
; DI unsigned pk_bf16(float lo, float hi) { f32x2 v = {lo, hi}; hbf16x2 r = __builtin_convertvector(v, hbf16x2); return __builtin_bit_cast(unsigned, r); }
;     DI void operator()(const f32x4 (&acc)[2][2][4][2], const pg8::GU& u, int wr, int wc, int fr, int fq) const {
;     ...
; #pragma unroll
;             for (int ai = 0; ai < 2; ++ai)
; #pragma unroll
;                 for (int m = 0; m < 4; ++m) {
;                     const int row = row0 + ai * 128 + m * 16;
;                     f32x4 x1 = acc[ai][bj][m][0], x2 = acc[ai][bj][m][1];
;                     if (MODE == 0) { x1 *= 0.07216878364870322f * LOG2E; x2 *= 0.07216878364870322f * LOG2E; }
;                     if (rot && row >= NCTX) {
;                         const int t = (row - NCTX) & (SEQ - 1), pos = axis ? (t & 63) : (t >> 6);
;                         const f32x2* cs = R + pos * (MODE == 0 ? 16 : 32) + ibase;
;                         f32x4 o1, o2;
; #pragma unroll
;                         for (int j = 0; j < 4; ++j) { const f32x2 c = cs[j]; o1[j] = x1[j] * c[0] - x2[j] * c[1]; o2[j] = x2[j] * c[0] + x1[j] * c[1]; }
;                         x1 = o1; x2 = o2;
;                     }
;                     bf16_t* rowp = O + (size_t)row * ldc + col0;
;                     u32x2 w1, w2; w1.x = pk_bf16(x1[0], x1[1]); w1.y = pk_bf16(x1[2], x1[3]); w2.x = pk_bf16(x2[0], x2[1]); w2.y = pk_bf16(x2[2], x2[3]);
;                     *(u32x2*)(rowp) = w1; *(u32x2*)(rowp + 16) = w2;
;                 }
.LBB0_445:
	s_or_b64 exec, exec, s[8:9]
	v_lshl_add_u64 v[60:61], v[58:59], 1, v[114:115]
	v_cvt_pk_bf16_f32 v54, v54, v55
	v_cvt_pk_bf16_f32 v55, v56, v57
	v_pk_mul_f32 v[48:49], v[48:49], s[54:55] op_sel_hi:[1,0]
	v_pk_mul_f32 v[46:47], v[46:47], s[54:55] op_sel_hi:[1,0]
	v_pk_mul_f32 v[44:45], v[44:45], s[54:55] op_sel_hi:[1,0]
	v_pk_mul_f32 v[42:43], v[42:43], s[54:55] op_sel_hi:[1,0]
	s_and_b64 s[8:9], s[72:73], s[4:5]
	v_cvt_pk_bf16_f32 v50, v50, v51
	v_cvt_pk_bf16_f32 v51, v52, v53
	global_store_dwordx2 v[60:61], v[54:55], off
	global_store_dwordx2 v[60:61], v[50:51], off offset:32
	s_and_saveexec_b64 s[4:5], s[8:9]
	s_cbranch_execz .LBB0_447
	s_waitcnt vmcnt(14)
	v_mul_f32_e32 v62, v48, v198
	v_mul_f32_e32 v64, v44, v199
	v_mul_f32_e32 v50, v44, v198
	v_mov_b32_e32 v44, v49
	v_mov_b32_e32 v61, v196
	v_mov_b32_e32 v56, v195
	v_mul_f32_e32 v68, v48, v199
	v_pk_mul_f32 v[70:71], v[44:45], v[200:201]
	v_mov_b32_e32 v48, v45
	v_mov_b32_e32 v60, v194
	v_mov_b32_e32 v57, v197
	v_pk_mul_f32 v[54:55], v[42:43], v[56:57]
	v_mov_b32_e32 v63, v70
	v_mov_b32_e32 v65, v71
	v_pk_mul_f32 v[44:45], v[48:49], v[200:201]
	v_pk_mul_f32 v[56:57], v[46:47], v[56:57]
	v_pk_fma_f32 v[46:47], v[46:47], v[60:61], v[54:55] neg_lo:[0,0,1] neg_hi:[0,0,1]
	v_pk_add_f32 v[54:55], v[62:63], v[64:65] neg_lo:[0,1] neg_hi:[0,1]
	v_mov_b32_e32 v51, v44
	v_mov_b32_e32 v69, v45
	v_pk_fma_f32 v[42:43], v[42:43], v[60:61], v[56:57]
	v_pk_add_f32 v[44:45], v[50:51], v[68:69]
	v_mov_b32_e32 v48, v54
	v_mov_b32_e32 v49, v55
.LBB0_447:
	s_or_b64 exec, exec, s[4:5]
	v_lshl_add_u64 v[50:51], v[58:59], 1, v[106:107]
	v_cvt_pk_bf16_f32 v46, v46, v47
	v_cvt_pk_bf16_f32 v47, v48, v49
	v_pk_mul_f32 v[40:41], v[40:41], s[54:55] op_sel_hi:[1,0]
	v_pk_mul_f32 v[38:39], v[38:39], s[54:55] op_sel_hi:[1,0]
	v_pk_mul_f32 v[36:37], v[36:37], s[54:55] op_sel_hi:[1,0]
	v_pk_mul_f32 v[34:35], v[34:35], s[54:55] op_sel_hi:[1,0]
	s_and_b64 s[8:9], s[72:73], vcc
	v_cvt_pk_bf16_f32 v42, v42, v43
	v_cvt_pk_bf16_f32 v43, v44, v45
	global_store_dwordx2 v[50:51], v[46:47], off
	global_store_dwordx2 v[50:51], v[42:43], off offset:32
	s_and_saveexec_b64 s[4:5], s[8:9]
	s_cbranch_execz .LBB0_449
	s_waitcnt vmcnt(14)
	v_mov_b32_e32 v50, v202
	v_mul_f32_e32 v42, v40, v206
	v_mul_f32_e32 v52, v36, v207
	v_mul_f32_e32 v46, v36, v206
	v_mul_f32_e32 v54, v40, v207
	v_mov_b32_e32 v36, v41
	v_mov_b32_e32 v40, v37
	v_mov_b32_e32 v51, v204
	v_mov_b32_e32 v44, v203
	v_pk_mul_f32 v[36:37], v[36:37], v[208:209]
	v_pk_mul_f32 v[40:41], v[40:41], v[208:209]
	v_mov_b32_e32 v45, v205
	v_pk_mul_f32 v[56:57], v[34:35], v[44:45]
	v_pk_mul_f32 v[44:45], v[38:39], v[44:45]
	v_mov_b32_e32 v43, v36
	v_mov_b32_e32 v53, v37
	v_mov_b32_e32 v47, v40
	v_mov_b32_e32 v55, v41
	v_pk_fma_f32 v[38:39], v[38:39], v[50:51], v[56:57] neg_lo:[0,0,1] neg_hi:[0,0,1]
	v_pk_fma_f32 v[34:35], v[34:35], v[50:51], v[44:45]
	v_pk_add_f32 v[40:41], v[42:43], v[52:53] neg_lo:[0,1] neg_hi:[0,1]
	v_pk_add_f32 v[36:37], v[46:47], v[54:55]
.LBB0_449:
	s_or_b64 exec, exec, s[4:5]
	v_lshl_add_u64 v[42:43], v[58:59], 1, v[98:99]
	v_cvt_pk_bf16_f32 v38, v38, v39
	v_cvt_pk_bf16_f32 v39, v40, v41
	v_pk_mul_f32 v[32:33], v[32:33], s[54:55] op_sel_hi:[1,0]
	v_pk_mul_f32 v[30:31], v[30:31], s[54:55] op_sel_hi:[1,0]
	v_pk_mul_f32 v[28:29], v[28:29], s[54:55] op_sel_hi:[1,0]
	v_pk_mul_f32 v[26:27], v[26:27], s[54:55] op_sel_hi:[1,0]
	s_and_b64 s[6:7], s[72:73], s[6:7]
	v_cvt_pk_bf16_f32 v34, v34, v35
	v_cvt_pk_bf16_f32 v35, v36, v37
	global_store_dwordx2 v[42:43], v[38:39], off
	global_store_dwordx2 v[42:43], v[34:35], off offset:32
	s_and_saveexec_b64 s[4:5], s[6:7]
	s_cbranch_execz .LBB0_451
	s_waitcnt vmcnt(14)
	v_mov_b32_e32 v42, v210
	v_mul_f32_e32 v34, v32, v214
	v_mul_f32_e32 v44, v28, v215
	v_mul_f32_e32 v38, v28, v214
	v_mul_f32_e32 v46, v32, v215
	v_mov_b32_e32 v28, v33
	v_mov_b32_e32 v32, v29
	v_mov_b32_e32 v43, v212
	v_mov_b32_e32 v36, v211
	v_pk_mul_f32 v[28:29], v[28:29], v[216:217]
	v_pk_mul_f32 v[32:33], v[32:33], v[216:217]
	v_mov_b32_e32 v37, v213
	v_pk_mul_f32 v[48:49], v[26:27], v[36:37]
	v_pk_mul_f32 v[36:37], v[30:31], v[36:37]
	v_mov_b32_e32 v35, v28
	v_mov_b32_e32 v45, v29
	v_mov_b32_e32 v39, v32
	v_mov_b32_e32 v47, v33
	v_pk_fma_f32 v[30:31], v[30:31], v[42:43], v[48:49] neg_lo:[0,0,1] neg_hi:[0,0,1]
	v_pk_fma_f32 v[26:27], v[26:27], v[42:43], v[36:37]
	v_pk_add_f32 v[32:33], v[34:35], v[44:45] neg_lo:[0,1] neg_hi:[0,1]
	v_pk_add_f32 v[28:29], v[38:39], v[46:47]
; DI unsigned pk_bf16(float lo, float hi) { f32x2 v = {lo, hi}; hbf16x2 r = __builtin_convertvector(v, hbf16x2); return __builtin_bit_cast(unsigned, r); }
;     DI void operator()(const f32x4 (&acc)[2][2][4][2], const pg8::GU& u, int wr, int wc, int fr, int fq) const {
;     ...
; #pragma unroll
;             for (int ai = 0; ai < 2; ++ai)
; #pragma unroll
;                 for (int m = 0; m < 4; ++m) {
;                     const int row = row0 + ai * 128 + m * 16;
;                     f32x4 x1 = acc[ai][bj][m][0], x2 = acc[ai][bj][m][1];
;                     if (MODE == 0) { x1 *= 0.07216878364870322f * LOG2E; x2 *= 0.07216878364870322f * LOG2E; }
;                     if (rot && row >= NCTX) {
;                         const int t = (row - NCTX) & (SEQ - 1), pos = axis ? (t & 63) : (t >> 6);
;                         const f32x2* cs = R + pos * (MODE == 0 ? 16 : 32) + ibase;
;                         f32x4 o1, o2;
; #pragma unroll
;                         for (int j = 0; j < 4; ++j) { const f32x2 c = cs[j]; o1[j] = x1[j] * c[0] - x2[j] * c[1]; o2[j] = x2[j] * c[0] + x1[j] * c[1]; }
;                         x1 = o1; x2 = o2;
;                     }
;                     bf16_t* rowp = O + (size_t)row * ldc + col0;
;                     u32x2 w1, w2; w1.x = pk_bf16(x1[0], x1[1]); w1.y = pk_bf16(x1[2], x1[3]); w2.x = pk_bf16(x2[0], x2[1]); w2.y = pk_bf16(x2[2], x2[3]);
;                     *(u32x2*)(rowp) = w1; *(u32x2*)(rowp + 16) = w2;
;                 }
.LBB0_451:
	s_or_b64 exec, exec, s[4:5]
	v_lshl_add_u64 v[34:35], v[58:59], 1, v[90:91]
	v_cvt_pk_bf16_f32 v30, v30, v31
	v_cvt_pk_bf16_f32 v31, v32, v33
	v_pk_mul_f32 v[24:25], v[24:25], s[54:55] op_sel_hi:[1,0]
	v_pk_mul_f32 v[22:23], v[22:23], s[54:55] op_sel_hi:[1,0]
	v_pk_mul_f32 v[20:21], v[20:21], s[54:55] op_sel_hi:[1,0]
	v_pk_mul_f32 v[18:19], v[18:19], s[54:55] op_sel_hi:[1,0]
	s_and_b64 s[6:7], s[72:73], s[10:11]
	v_cvt_pk_bf16_f32 v26, v26, v27
	v_cvt_pk_bf16_f32 v27, v28, v29
	global_store_dwordx2 v[34:35], v[30:31], off
	global_store_dwordx2 v[34:35], v[26:27], off offset:32
	s_and_saveexec_b64 s[4:5], s[6:7]
	s_cbranch_execz .LBB0_453
	s_waitcnt vmcnt(14)
	v_mov_b32_e32 v34, v224
	v_mul_f32_e32 v26, v24, v228
	v_mul_f32_e32 v36, v20, v229
	v_mul_f32_e32 v30, v20, v228
	v_mul_f32_e32 v38, v24, v229
	v_mov_b32_e32 v20, v25
	v_mov_b32_e32 v24, v21
	v_mov_b32_e32 v35, v226
	v_mov_b32_e32 v28, v225
	v_pk_mul_f32 v[20:21], v[20:21], v[230:231]
	v_pk_mul_f32 v[24:25], v[24:25], v[230:231]
	v_mov_b32_e32 v29, v227
	v_pk_mul_f32 v[40:41], v[18:19], v[28:29]
	v_pk_mul_f32 v[28:29], v[22:23], v[28:29]
	v_mov_b32_e32 v27, v20
	v_mov_b32_e32 v37, v21
	v_mov_b32_e32 v31, v24
	v_mov_b32_e32 v39, v25
	v_pk_fma_f32 v[22:23], v[22:23], v[34:35], v[40:41] neg_lo:[0,0,1] neg_hi:[0,0,1]
	v_pk_fma_f32 v[18:19], v[18:19], v[34:35], v[28:29]
	v_pk_add_f32 v[24:25], v[26:27], v[36:37] neg_lo:[0,1] neg_hi:[0,1]
	v_pk_add_f32 v[20:21], v[30:31], v[38:39]
.LBB0_453:
	s_or_b64 exec, exec, s[4:5]
	v_lshl_add_u64 v[26:27], v[58:59], 1, v[82:83]
	v_cvt_pk_bf16_f32 v22, v22, v23
	v_cvt_pk_bf16_f32 v23, v24, v25
	v_pk_mul_f32 v[16:17], v[16:17], s[54:55] op_sel_hi:[1,0]
	v_pk_mul_f32 v[14:15], v[14:15], s[54:55] op_sel_hi:[1,0]
	v_pk_mul_f32 v[12:13], v[12:13], s[54:55] op_sel_hi:[1,0]
	v_pk_mul_f32 v[10:11], v[10:11], s[54:55] op_sel_hi:[1,0]
	s_and_b64 s[6:7], s[72:73], s[14:15]
	v_cvt_pk_bf16_f32 v18, v18, v19
	v_cvt_pk_bf16_f32 v19, v20, v21
	global_store_dwordx2 v[26:27], v[22:23], off
	global_store_dwordx2 v[26:27], v[18:19], off offset:32
	s_and_saveexec_b64 s[4:5], s[6:7]
	s_cbranch_execz .LBB0_455
	s_waitcnt vmcnt(14)
	v_mov_b32_e32 v26, v232
	v_mul_f32_e32 v18, v16, v236
	v_mul_f32_e32 v28, v12, v237
	v_mul_f32_e32 v22, v12, v236
	v_mul_f32_e32 v30, v16, v237
	v_mov_b32_e32 v12, v17
	v_mov_b32_e32 v16, v13
	v_mov_b32_e32 v27, v234
	v_mov_b32_e32 v20, v233
	v_pk_mul_f32 v[12:13], v[12:13], v[238:239]
	v_pk_mul_f32 v[16:17], v[16:17], v[238:239]
	v_mov_b32_e32 v21, v235
	v_pk_mul_f32 v[32:33], v[10:11], v[20:21]
	v_pk_mul_f32 v[20:21], v[14:15], v[20:21]
	v_mov_b32_e32 v19, v12
	v_mov_b32_e32 v29, v13
	v_mov_b32_e32 v23, v16
	v_mov_b32_e32 v31, v17
	v_pk_fma_f32 v[14:15], v[14:15], v[26:27], v[32:33] neg_lo:[0,0,1] neg_hi:[0,0,1]
	v_pk_fma_f32 v[10:11], v[10:11], v[26:27], v[20:21]
	v_pk_add_f32 v[16:17], v[18:19], v[28:29] neg_lo:[0,1] neg_hi:[0,1]
	v_pk_add_f32 v[12:13], v[22:23], v[30:31]
.LBB0_455:
	s_or_b64 exec, exec, s[4:5]
	v_lshl_add_u64 v[18:19], v[58:59], 1, v[74:75]
	v_cvt_pk_bf16_f32 v14, v14, v15
	v_cvt_pk_bf16_f32 v15, v16, v17
	v_pk_mul_f32 v[8:9], v[8:9], s[54:55] op_sel_hi:[1,0]
	v_pk_mul_f32 v[6:7], v[6:7], s[54:55] op_sel_hi:[1,0]
	v_pk_mul_f32 v[4:5], v[4:5], s[54:55] op_sel_hi:[1,0]
	v_pk_mul_f32 v[2:3], v[2:3], s[54:55] op_sel_hi:[1,0]
	s_and_b64 s[6:7], s[72:73], s[16:17]
	v_cvt_pk_bf16_f32 v10, v10, v11
	v_cvt_pk_bf16_f32 v11, v12, v13
	global_store_dwordx2 v[18:19], v[14:15], off
	global_store_dwordx2 v[18:19], v[10:11], off offset:32
	s_and_saveexec_b64 s[4:5], s[6:7]
	s_cbranch_execz .LBB0_457
	s_waitcnt vmcnt(14)
	v_mov_b32_e32 v18, v240
	v_mul_f32_e32 v10, v8, v244
	v_mul_f32_e32 v20, v4, v245
	v_mul_f32_e32 v14, v4, v244
	v_mul_f32_e32 v22, v8, v245
	v_mov_b32_e32 v4, v9
	v_mov_b32_e32 v8, v5
	v_mov_b32_e32 v19, v242
	v_mov_b32_e32 v12, v241
	v_pk_mul_f32 v[4:5], v[4:5], v[246:247]
	v_pk_mul_f32 v[8:9], v[8:9], v[246:247]
	v_mov_b32_e32 v13, v243
	v_pk_mul_f32 v[24:25], v[2:3], v[12:13]
	v_pk_mul_f32 v[12:13], v[6:7], v[12:13]
	v_mov_b32_e32 v11, v4
	v_mov_b32_e32 v21, v5
	v_mov_b32_e32 v15, v8
	v_mov_b32_e32 v23, v9
	v_pk_fma_f32 v[6:7], v[6:7], v[18:19], v[24:25] neg_lo:[0,0,1] neg_hi:[0,0,1]
	v_pk_fma_f32 v[2:3], v[2:3], v[18:19], v[12:13]
	v_pk_add_f32 v[8:9], v[10:11], v[20:21] neg_lo:[0,1] neg_hi:[0,1]
	v_pk_add_f32 v[4:5], v[14:15], v[22:23]
